# speedup vs baseline: 1.0144x; 1.0085x over previous
.LBB13_6:
	s_or_b64 exec, exec, s[14:15]
	s_and_b32 s14, s3, 3
	v_lshl_or_b32 v80, s14, 14, v10
	s_waitcnt vmcnt(0)
	s_waitcnt lgkmcnt(0)
	s_barrier
	ds_read_b128 v[10:13], v80
	ds_read_b128 v[14:17], v80 offset:1024
	ds_read_b128 v[56:59], v80 offset:8192
	ds_read_b128 v[60:63], v80 offset:9216
	v_and_b32_e32 v98, 31, v0
	v_lshlrev_b32_e32 v82, 2, v98
	s_waitcnt lgkmcnt(2)
	v_mfma_f32_32x32x64_f8f6f4 v[16:31], v[10:17], v[2:9], 0
	ds_read_b128 v[64:67], v80 offset:2048
	ds_read_b128 v[68:71], v80 offset:3072
	ds_read_b128 v[72:75], v80 offset:10240
	ds_read_b128 v[76:79], v80 offset:11264
	s_lshr_b32 s16, s2, 3
	s_lshl_b32 s3, s21, 14
	s_and_b32 s16, s16, 0x1fffffe0
	s_add_i32 s3, s3, s16
	s_lshl_b32 s15, s14, 12
	s_add_i32 s3, s3, s19
	s_lshr_b32 s2, s2, 2
	v_lshrrev_b32_e32 v81, 5, v109
	s_and_b32 s2, s2, 32
	v_lshlrev_b32_e32 v111, 2, v81
	v_lshl_or_b32 v97, s14, 6, v111
	v_lshl_or_b32 v96, v81, 16, v82
	s_load_dwordx2 s[0:1], s[0:1], 0x70
	s_waitcnt lgkmcnt(0)
	v_mfma_f32_32x32x64_f8f6f4 v[0:15], v[56:63], v[2:9], 0
	ds_read_b128 v[88:91], v80 offset:4096
	ds_read_b128 v[92:95], v80 offset:5120
	ds_read_b128 v[114:117], v80 offset:12288
	ds_read_b128 v[118:121], v80 offset:13312
	ds_read_b128 v[100:103], v80 offset:6144
	ds_read_b128 v[104:107], v80 offset:7168
	ds_read_b128 v[56:59], v80 offset:14336
	ds_read_b128 v[60:63], v80 offset:15360
	s_waitcnt lgkmcnt(0)
	s_barrier
	global_load_dword v112, v82, s[8:9]
	global_load_dword v113, v82, s[10:11]
	s_add_i32 s8, s3, s15
	s_mov_b32 s9, 0
	s_lshl_b64 s[8:9], s[8:9], 6
	s_or_b32 s8, s8, s2
	s_lshl_b64 s[2:3], s[8:9], 2
	s_add_u32 s8, s12, s2
	v_lshlrev_b32_e32 v80, 2, v97
	s_addc_u32 s9, s13, s3
	s_lshl_b32 s10, s19, 2
	s_load_dword s4, s[4:5], s10 offset:0x0
	s_nop 0
	s_load_dword s5, s[6:7], s10 offset:0x0
	v_mfma_f32_32x32x64_f8f6f4 v[0:15], v[72:79], v[48:55], v[0:15]
	v_or_b32_e32 v99, 0x10800, v80
	v_or_b32_e32 v123, 0x11000, v80
	v_or_b32_e32 v124, 0x11800, v80
	v_or_b32_e32 v122, 0x10c00, v80
	v_or_b32_e32 v125, 0x11400, v80
	s_mul_i32 s6, s18, 0xa00
	v_mfma_f32_32x32x64_f8f6f4 v[16:31], v[64:71], v[48:55], v[16:31]
	v_or_b32_e32 v48, 0x10000, v80
	v_or_b32_e32 v49, 0x10400, v80
	ds_read_b128 v[52:55], v48
	ds_read_b128 v[84:87], v49
	v_mov_b32_e32 v48, v96
	ds_read_b128 v[64:67], v99
	ds_read_b128 v[68:71], v122
	ds_read_b128 v[72:75], v123
	ds_read_b128 v[76:79], v125
	ds_read_b128 v[80:83], v124
	global_load_dword v110, v48, s[8:9] nt
	v_add_u32_e32 v49, 0x4000, v48
	v_mfma_f32_32x32x64_f8f6f4 v[0:15], v[114:121], v[40:47], v[0:15]
	global_load_dword v120, v49, s[8:9] nt
	s_waitcnt lgkmcnt(0)
	v_mov_b32_e32 v114, s5
	v_mul_f32_e32 v114, 0xbfb8aa3b, v114
	v_mov_b32_e32 v108, 0xbfb8aa3b
	v_mul_f32_e32 v108, s4, v108
	s_nop 1
	v_readfirstlane_b32 s4, v108
	s_nop 1
	v_mfma_f32_32x32x64_f8f6f4 v[16:31], v[88:95], v[40:47], v[16:31]
	s_add_u32 s40, s8, 0x8000
	s_addc_u32 s41, s9, 0
	global_load_dword v121, v48, s[40:41] nt
	s_add_u32 s40, s8, 0xc000
	s_addc_u32 s41, s9, 0
	global_load_dword v126, v48, s[40:41] nt
	v_mfma_f32_32x32x64_f8f6f4 v[16:31], v[100:107], v[32:39], v[16:31]
	v_fma_f32 v100, s4, v84, v114
	s_waitcnt vmcnt(4)
	v_fma_f32 v101, v112, v84, v113
	v_or_b32_e32 v84, 8, v97
	v_lshlrev_b32_e32 v102, 2, v84
	v_or_b32_e32 v40, 0x10000, v102
	v_or_b32_e32 v41, 0x10400, v102
	v_or_b32_e32 v104, 0x10800, v102
	v_or_b32_e32 v106, 0x11000, v102
	v_or_b32_e32 v108, 0x11800, v102
	ds_read_b128 v[92:95], v40
	ds_read_b128 v[88:91], v41
	v_or_b32_e32 v105, 0x10c00, v102
	ds_read_b128 v[40:43], v104
	ds_read_b128 v[44:47], v105
	v_mfma_f32_32x32x64_f8f6f4 v[0:15], v[56:63], v[32:39], v[0:15]
	v_mov_b32_e32 v56, v96
	v_or_b32_e32 v107, 0x11400, v102
	ds_read_b128 v[48:51], v106
	ds_read_b128 v[32:35], v107
	ds_read_b128 v[36:39], v108
	v_mul_f32_e32 v58, v100, v101
	s_add_u32 s40, s8, 0x20000
	s_addc_u32 s41, s9, 0
	global_load_dword v57, v56, s[40:41] nt
	s_add_u32 s40, s8, 0x24000
	s_addc_u32 s41, s9, 0
	global_load_dword v59, v56, s[40:41] nt
	s_add_u32 s40, s8, 0x28000
	s_addc_u32 s41, s9, 0
	global_load_dword v60, v56, s[40:41] nt
	v_add_u32_e32 v56, 0x2c000, v56
	global_load_dword v56, v56, s[8:9] nt
	s_add_u32 s40, s8, 0x40000
	s_addc_u32 s41, s9, 0
	global_load_dword v100, v96, s[40:41] nt
	s_add_u32 s40, s8, 0x44000
	s_addc_u32 s41, s9, 0
	global_load_dword v101, v96, s[40:41] nt
	s_add_u32 s40, s8, 0x48000
	s_addc_u32 s41, s9, 0
	global_load_dword v102, v96, s[40:41] nt
	s_add_u32 s40, s8, 0x4c000
	s_addc_u32 s41, s9, 0
	global_load_dword v103, v96, s[40:41] nt
	v_exp_f32_e32 v58, v58
	v_fmamk_f32 v16, v16, 0x39800000, v52
	v_fma_f32 v52, v112, v85, v113
	v_fmamk_f32 v17, v17, 0x39800000, v53
	v_add_f32_e32 v58, 1.0, v58
	v_rcp_f32_e32 v58, v58
	v_fmac_f32_e32 v55, 0x39800000, v19
	s_waitcnt lgkmcnt(5)
	v_fma_f32 v19, v112, v89, v113
	v_fmac_f32_e32 v95, 0x39800000, v23
	s_waitcnt vmcnt(11)
	v_add_f32_e32 v16, v16, v110
	v_mul_f32_e32 v110, v16, v58
	v_fma_f32 v16, s4, v85, v114
	v_mul_f32_e32 v16, v16, v52
	v_exp_f32_e32 v16, v16
	v_fma_f32 v117, v72, v110, 0
	v_fma_f32 v118, v76, v110, 0
	s_waitcnt vmcnt(10)
	v_add_f32_e32 v17, v17, v120
	v_add_f32_e32 v16, 1.0, v16
	v_rcp_f32_e32 v16, v16
	v_fma_f32 v119, v80, v110, 0
	v_fma_f32 v115, v64, v110, 0
	v_fma_f32 v116, v68, v110, 0
	v_mul_f32_e32 v72, v17, v16
	v_fma_f32 v16, s4, v86, v114
	v_fma_f32 v17, v112, v86, v113
	v_mul_f32_e32 v16, v16, v17
	v_exp_f32_e32 v16, v16
	v_fmamk_f32 v17, v18, 0x39800000, v54
	v_fmac_f32_e32 v117, v73, v72
	v_fma_f32 v18, v112, v88, v113
	v_add_f32_e32 v16, 1.0, v16
	v_rcp_f32_e32 v16, v16
	s_waitcnt vmcnt(9)
	v_add_f32_e32 v17, v17, v121
	v_fmac_f32_e32 v118, v77, v72
	v_fmac_f32_e32 v119, v81, v72
	v_mul_f32_e32 v73, v17, v16
	v_fma_f32 v16, s4, v87, v114
	v_fma_f32 v17, v112, v87, v113
	v_mul_f32_e32 v16, v16, v17
	v_exp_f32_e32 v16, v16
	s_waitcnt vmcnt(8)
	v_add_f32_e32 v17, v55, v126
	v_fmac_f32_e32 v117, v74, v73
	v_or_b32_e32 v77, 16, v97
	v_add_f32_e32 v16, 1.0, v16
	v_rcp_f32_e32 v16, v16
	v_fmac_f32_e32 v115, v65, v72
	v_fmac_f32_e32 v116, v69, v72
	v_fmac_f32_e32 v119, v82, v73
	v_mul_f32_e32 v74, v17, v16
	v_fma_f32 v17, s4, v88, v114
	v_mul_f32_e32 v17, v17, v18
	v_fma_f32 v18, s4, v89, v114
	v_exp_f32_e32 v17, v17
	v_mul_f32_e32 v18, v18, v19
	v_exp_f32_e32 v18, v18
	v_add_f32_e32 v17, 1.0, v17
	v_rcp_f32_e32 v17, v17
	v_fmamk_f32 v16, v20, 0x39800000, v92
	v_add_f32_e32 v18, 1.0, v18
	v_rcp_f32_e32 v18, v18
	v_fmac_f32_e32 v117, v75, v74
	v_lshlrev_b32_e32 v52, 2, v77
	v_fmac_f32_e32 v115, v66, v73
	v_fmac_f32_e32 v116, v70, v73
	v_fmac_f32_e32 v118, v78, v73
	v_fmac_f32_e32 v119, v83, v74
	v_fma_f32 v85, s4, v90, v114
	s_waitcnt vmcnt(7)
	v_add_f32_e32 v16, v16, v57
	v_mul_f32_e32 v76, v16, v17
	v_fmamk_f32 v16, v21, 0x39800000, v93
	s_waitcnt vmcnt(6)
	v_add_f32_e32 v16, v16, v59
	v_mul_f32_e32 v75, v16, v18
	v_fmamk_f32 v16, v22, 0x39800000, v94
	s_waitcnt vmcnt(5)
	v_add_f32_e32 v83, v16, v60
	v_fma_f32 v86, v112, v90, v113
	v_or_b32_e32 v16, 0x10000, v52
	v_or_b32_e32 v17, 0x10400, v52
	v_or_b32_e32 v78, 0x10800, v52
	v_or_b32_e32 v80, 0x11000, v52
	v_or_b32_e32 v82, 0x11800, v52
	v_mov_b32_e32 v90, v96
	v_fmac_f32_e32 v115, v67, v74
	v_fmac_f32_e32 v116, v71, v74
	v_fmac_f32_e32 v118, v79, v74
	s_waitcnt vmcnt(4)
	v_add_f32_e32 v87, v95, v56
	v_fma_f32 v88, s4, v91, v114
	v_fma_f32 v89, v112, v91, v113
	ds_read_b128 v[56:59], v16
	ds_read_b128 v[68:71], v17
	v_or_b32_e32 v79, 0x10c00, v52
	ds_read_b128 v[64:67], v78
	ds_read_b128 v[60:63], v79
	v_or_b32_e32 v81, 0x11400, v52
	ds_read_b128 v[16:19], v80
	ds_read_b128 v[20:23], v81
	ds_read_b128 v[52:55], v82
	v_mul_f32_e32 v85, v85, v86
	v_mul_f32_e32 v88, v88, v89
	s_add_u32 s40, s8, 0x60000
	s_addc_u32 s41, s9, 0
	global_load_dword v120, v96, s[40:41] nt
	s_add_u32 s40, s8, 0x64000
	s_addc_u32 s41, s9, 0
	global_load_dword v121, v96, s[40:41] nt
	s_add_u32 s40, s8, 0x68000
	s_addc_u32 s41, s9, 0
	global_load_dword v126, v96, s[40:41] nt
	s_add_u32 s40, s8, 0x6c000
	s_addc_u32 s41, s9, 0
	global_load_dword v92, v96, s[40:41] nt
	s_waitcnt lgkmcnt(8)
	v_fmac_f32_e32 v118, v32, v76
	v_exp_f32_e32 v32, v85
	v_fmac_f32_e32 v118, v33, v75
	v_exp_f32_e32 v33, v88
	v_add_f32_e32 v32, 1.0, v32
	v_rcp_f32_e32 v32, v32
	s_waitcnt lgkmcnt(6)
	v_fmamk_f32 v24, v24, 0x39800000, v56
	v_fmac_f32_e32 v116, v44, v76
	v_fmac_f32_e32 v116, v45, v75
	v_mul_f32_e32 v85, v83, v32
	v_add_f32_e32 v32, 1.0, v33
	v_rcp_f32_e32 v32, v32
	s_waitcnt lgkmcnt(5)
	v_fma_f32 v33, v112, v68, v113
	v_fmac_f32_e32 v118, v34, v85
	v_fma_f32 v34, v112, v69, v113
	v_mul_f32_e32 v83, v87, v32
	v_fma_f32 v32, s4, v68, v114
	v_mul_f32_e32 v32, v32, v33
	v_exp_f32_e32 v32, v32
	v_fma_f32 v33, s4, v69, v114
	v_mul_f32_e32 v33, v33, v34
	v_add_f32_e32 v32, 1.0, v32
	v_rcp_f32_e32 v32, v32
	v_exp_f32_e32 v33, v33
	v_fmac_f32_e32 v116, v46, v85
	v_fmamk_f32 v25, v25, 0x39800000, v57
	v_fmac_f32_e32 v116, v47, v83
	v_fmac_f32_e32 v115, v40, v76
	v_fmac_f32_e32 v115, v41, v75
	v_fmac_f32_e32 v115, v42, v85
	v_fmac_f32_e32 v115, v43, v83
	v_fmac_f32_e32 v59, 0x39800000, v27
	v_fmac_f32_e32 v117, v48, v76
	v_fmac_f32_e32 v119, v36, v76
	v_fmac_f32_e32 v117, v49, v75
	v_fmac_f32_e32 v119, v37, v75
	v_fmac_f32_e32 v117, v50, v85
	v_fmac_f32_e32 v119, v38, v85
	v_fmac_f32_e32 v117, v51, v83
	v_fmac_f32_e32 v118, v35, v83
	v_fmac_f32_e32 v119, v39, v83
	v_mov_b32_e32 v94, v96
	s_waitcnt vmcnt(7)
	v_add_f32_e32 v24, v24, v100
	v_mul_f32_e32 v68, v24, v32
	v_add_f32_e32 v24, 1.0, v33
	v_rcp_f32_e32 v24, v24
	s_waitcnt vmcnt(6)
	v_add_f32_e32 v25, v25, v101
	s_waitcnt lgkmcnt(3)
	v_fmac_f32_e32 v116, v60, v68
	v_fma_f32 v32, v112, v71, v113
	v_mul_f32_e32 v60, v25, v24
	v_fma_f32 v24, s4, v70, v114
	v_fma_f32 v25, v112, v70, v113
	v_mul_f32_e32 v24, v24, v25
	v_exp_f32_e32 v24, v24
	v_fmamk_f32 v25, v26, 0x39800000, v58
	v_fma_f32 v26, s4, v71, v114
	v_mul_f32_e32 v26, v26, v32
	v_add_f32_e32 v24, 1.0, v24
	v_rcp_f32_e32 v24, v24
	v_exp_f32_e32 v26, v26
	s_waitcnt vmcnt(5)
	v_add_f32_e32 v25, v25, v102
	v_fmac_f32_e32 v115, v64, v68
	v_mul_f32_e32 v64, v25, v24
	v_add_f32_e32 v24, 1.0, v26
	v_rcp_f32_e32 v24, v24
	v_fmac_f32_e32 v116, v61, v60
	v_fmac_f32_e32 v116, v62, v64
	s_waitcnt vmcnt(4)
	v_add_f32_e32 v25, v59, v103
	v_or_b32_e32 v62, 24, v97
	v_fmac_f32_e32 v115, v65, v60
	v_mul_f32_e32 v61, v25, v24
	v_lshlrev_b32_e32 v24, 2, v62
	v_fmac_f32_e32 v115, v66, v64
	v_fmac_f32_e32 v116, v63, v61
	v_or_b32_e32 v25, 0x10000, v24
	v_or_b32_e32 v26, 0x10400, v24
	v_or_b32_e32 v63, 0x10800, v24
	v_or_b32_e32 v66, 0x11000, v24
	v_or_b32_e32 v69, 0x11800, v24
	v_mov_b32_e32 v70, v96
	v_fmac_f32_e32 v115, v67, v61
	ds_read_b128 v[48:51], v25
	ds_read_b128 v[56:59], v26
	v_or_b32_e32 v65, 0x10c00, v24
	ds_read_b128 v[44:47], v63
	ds_read_b128 v[32:35], v65
	v_or_b32_e32 v67, 0x11400, v24
	ds_read_b128 v[36:39], v66
	ds_read_b128 v[40:43], v67
	ds_read_b128 v[24:27], v69
	s_waitcnt lgkmcnt(9)
	v_fmac_f32_e32 v117, v16, v68
	s_add_u32 s40, s8, 0x80000
	s_addc_u32 s41, s9, 0
	global_load_dword v95, v96, s[40:41] nt
	v_fmac_f32_e32 v117, v17, v60
	v_fmac_f32_e32 v117, v18, v64
	s_waitcnt lgkmcnt(5)
	v_fma_f32 v17, s4, v56, v114
	v_fma_f32 v18, v112, v56, v113
	v_mul_f32_e32 v17, v17, v18
	v_fmac_f32_e32 v117, v19, v61
	v_fma_f32 v18, s4, v57, v114
	v_fma_f32 v19, v112, v57, v113
	v_exp_f32_e32 v17, v17
	v_mul_f32_e32 v18, v18, v19
	v_exp_f32_e32 v18, v18
	v_add_f32_e32 v17, 1.0, v17
	v_rcp_f32_e32 v17, v17
	v_fmamk_f32 v16, v28, 0x39800000, v48
	v_add_f32_e32 v18, 1.0, v18
	v_rcp_f32_e32 v18, v18
	v_fma_f32 v19, v112, v59, v113
	v_fmac_f32_e32 v51, 0x39800000, v31
	v_fmac_f32_e32 v118, v20, v68
	v_fmac_f32_e32 v119, v52, v68
	v_fmac_f32_e32 v118, v21, v60
	v_fmac_f32_e32 v119, v53, v60
	v_fmac_f32_e32 v118, v22, v64
	v_fmac_f32_e32 v119, v54, v64
	v_fmac_f32_e32 v118, v23, v61
	v_fmac_f32_e32 v119, v55, v61
	s_waitcnt vmcnt(4)
	v_add_f32_e32 v16, v16, v120
	v_mul_f32_e32 v71, v16, v17
	v_fmamk_f32 v16, v29, 0x39800000, v49
	s_waitcnt vmcnt(3)
	v_add_f32_e32 v16, v16, v121
	v_mul_f32_e32 v70, v16, v18
	v_fma_f32 v17, s4, v58, v114
	v_fma_f32 v18, v112, v58, v113
	v_mul_f32_e32 v17, v17, v18
	v_fma_f32 v18, s4, v59, v114
	v_mul_f32_e32 v18, v18, v19
	v_exp_f32_e32 v17, v17
	v_exp_f32_e32 v18, v18
	v_fmamk_f32 v16, v30, 0x39800000, v50
	v_add_f32_e32 v17, 1.0, v17
	v_rcp_f32_e32 v17, v17
	v_add_f32_e32 v18, 1.0, v18
	v_rcp_f32_e32 v18, v18
	s_waitcnt vmcnt(2)
	v_add_f32_e32 v16, v16, v126
	v_mul_f32_e32 v88, v16, v17
	s_waitcnt vmcnt(1)
	v_add_f32_e32 v16, v51, v92
	v_or_b32_e32 v87, 32, v97
	v_mul_f32_e32 v86, v16, v18
	v_lshlrev_b32_e32 v16, 2, v87
	v_or_b32_e32 v17, 0x10000, v16
	v_or_b32_e32 v18, 0x10400, v16
	v_or_b32_e32 v89, 0x10800, v16
	v_or_b32_e32 v91, 0x11000, v16
	v_or_b32_e32 v93, 0x11800, v16
	ds_read_b128 v[28:31], v17
	ds_read_b128 v[100:103], v18
	v_or_b32_e32 v90, 0x10c00, v16
	ds_read_b128 v[52:55], v89
	ds_read_b128 v[48:51], v90
	v_or_b32_e32 v92, 0x11400, v16
	ds_read_b128 v[56:59], v91
	ds_read_b128 v[20:23], v92
	ds_read_b128 v[16:19], v93
	s_waitcnt lgkmcnt(11)
	v_fmac_f32_e32 v115, v44, v71
	s_add_u32 s40, s8, 0x84000
	s_addc_u32 s41, s9, 0
	global_load_dword v44, v94, s[40:41] nt
	v_fmac_f32_e32 v115, v45, v70
	s_add_u32 s40, s8, 0x88000
	s_addc_u32 s41, s9, 0
	global_load_dword v45, v94, s[40:41] nt
	v_fmac_f32_e32 v115, v46, v88
	s_add_u32 s40, s8, 0x8c000
	s_addc_u32 s41, s9, 0
	global_load_dword v46, v94, s[40:41] nt
	s_add_u32 s40, s8, 0xa0000
	s_addc_u32 s41, s9, 0
	global_load_dword v120, v96, s[40:41] nt
	s_add_u32 s40, s8, 0xa4000
	s_addc_u32 s41, s9, 0
	global_load_dword v121, v96, s[40:41] nt
	s_add_u32 s40, s8, 0xa8000
	s_addc_u32 s41, s9, 0
	global_load_dword v126, v96, s[40:41] nt
	s_waitcnt lgkmcnt(7)
	v_fmac_f32_e32 v119, v24, v71
	v_fmac_f32_e32 v119, v25, v70
	s_waitcnt lgkmcnt(5)
	v_fma_f32 v24, s4, v100, v114
	v_fma_f32 v25, v112, v100, v113
	v_mul_f32_e32 v24, v24, v25
	v_exp_f32_e32 v24, v24
	v_fmac_f32_e32 v119, v26, v88
	v_fma_f32 v25, s4, v101, v114
	v_fma_f32 v26, v112, v101, v113
	v_mul_f32_e32 v25, v25, v26
	v_add_f32_e32 v24, 1.0, v24
	v_rcp_f32_e32 v24, v24
	v_exp_f32_e32 v26, v25
	v_fmamk_f32 v0, v0, 0x39800000, v28
	v_fmamk_f32 v1, v1, 0x39800000, v29
	v_fmac_f32_e32 v116, v32, v71
	v_fmac_f32_e32 v117, v36, v71
	v_fmac_f32_e32 v116, v33, v70
	v_fmac_f32_e32 v117, v37, v70
	v_fmac_f32_e32 v116, v34, v88
	v_fmac_f32_e32 v117, v38, v88
	v_fmac_f32_e32 v115, v47, v86
	v_fmac_f32_e32 v116, v35, v86
	v_fmac_f32_e32 v117, v39, v86
	v_fmac_f32_e32 v119, v27, v86
	v_fmac_f32_e32 v31, 0x39800000, v3
	v_or_b32_e32 v27, 40, v97
	v_fmac_f32_e32 v118, v40, v71
	v_lshlrev_b32_e32 v33, 2, v27
	v_fmac_f32_e32 v118, v41, v70
	v_or_b32_e32 v29, 0x10400, v33
	v_fmac_f32_e32 v118, v42, v88
	v_or_b32_e32 v32, 0x11400, v33
	v_fmac_f32_e32 v118, v43, v86
	s_waitcnt vmcnt(6)
	v_add_f32_e32 v0, v0, v95
	v_mul_f32_e32 v25, v0, v24
	v_add_f32_e32 v0, 1.0, v26
	v_rcp_f32_e32 v0, v0
	s_waitcnt vmcnt(5)
	v_add_f32_e32 v1, v1, v44
	v_fma_f32 v26, v112, v103, v113
	s_waitcnt lgkmcnt(4)
	v_fmac_f32_e32 v115, v52, v25
	v_mul_f32_e32 v24, v1, v0
	v_fma_f32 v0, s4, v102, v114
	v_fma_f32 v1, v112, v102, v113
	v_mul_f32_e32 v0, v0, v1
	v_exp_f32_e32 v0, v0
	v_fmamk_f32 v1, v2, 0x39800000, v30
	v_fma_f32 v2, s4, v103, v114
	v_mul_f32_e32 v2, v2, v26
	s_add_u32 s40, s8, 0xac000
	s_addc_u32 s41, s9, 0
	global_load_dword v103, v96, s[40:41] nt
	v_add_f32_e32 v0, 1.0, v0
	v_rcp_f32_e32 v0, v0
	v_exp_f32_e32 v2, v2
	s_waitcnt vmcnt(5)
	v_add_f32_e32 v1, v1, v45
	s_waitcnt lgkmcnt(3)
	v_fmac_f32_e32 v116, v48, v25
	v_mul_f32_e32 v28, v1, v0
	v_add_f32_e32 v0, 1.0, v2
	v_rcp_f32_e32 v0, v0
	s_waitcnt lgkmcnt(2)
	v_fmac_f32_e32 v117, v56, v25
	s_waitcnt vmcnt(4)
	v_add_f32_e32 v1, v31, v46
	v_fmac_f32_e32 v115, v53, v24
	v_fmac_f32_e32 v116, v49, v24
	v_fmac_f32_e32 v117, v57, v24
	v_mul_f32_e32 v26, v1, v0
	v_or_b32_e32 v0, 0x10000, v33
	v_fmac_f32_e32 v115, v54, v28
	v_fmac_f32_e32 v116, v50, v28
	v_fmac_f32_e32 v117, v58, v28
	ds_read_b128 v[0:3], v0
	ds_read_b128 v[34:37], v29
	v_or_b32_e32 v29, 0x10800, v33
	v_or_b32_e32 v30, 0x10c00, v33
	v_or_b32_e32 v31, 0x11000, v33
	v_or_b32_e32 v33, 0x11800, v33
	v_mov_b32_e32 v58, v96
	v_fmac_f32_e32 v115, v55, v26
	v_fmac_f32_e32 v116, v51, v26
	v_fmac_f32_e32 v117, v59, v26
	ds_read_b128 v[38:41], v29
	ds_read_b128 v[42:45], v30
	ds_read_b128 v[46:49], v31
	ds_read_b128 v[50:53], v32
	ds_read_b128 v[54:57], v33
	s_waitcnt lgkmcnt(8)
	v_fmac_f32_e32 v118, v20, v25
	s_add_u32 s40, s8, 0xc4000
	s_addc_u32 s41, s9, 0
	global_load_dword v100, v96, s[40:41] nt
	s_add_u32 s40, s8, 0xc8000
	s_addc_u32 s41, s9, 0
	global_load_dword v101, v96, s[40:41] nt
	s_add_u32 s40, s8, 0xcc000
	s_addc_u32 s41, s9, 0
	global_load_dword v102, v96, s[40:41] nt
	v_fmac_f32_e32 v118, v21, v24
	s_waitcnt lgkmcnt(5)
	v_fma_f32 v20, s4, v34, v114
	v_fma_f32 v21, v112, v34, v113
	v_mul_f32_e32 v20, v20, v21
	v_exp_f32_e32 v20, v20
	v_fmac_f32_e32 v119, v16, v25
	v_fmamk_f32 v0, v4, 0x39800000, v0
	v_fma_f32 v4, v112, v35, v113
	v_add_f32_e32 v16, 1.0, v20
	v_rcp_f32_e32 v16, v16
	v_fmamk_f32 v1, v5, 0x39800000, v1
	v_fmac_f32_e32 v118, v22, v28
	v_fmac_f32_e32 v3, 0x39800000, v7
	v_or_b32_e32 v34, 48, v97
	v_fmac_f32_e32 v118, v23, v26
	v_fmac_f32_e32 v119, v17, v24
	v_fmac_f32_e32 v119, v18, v28
	v_fmac_f32_e32 v119, v19, v26
	s_waitcnt vmcnt(6)
	v_add_f32_e32 v0, v0, v120
	v_mul_f32_e32 v20, v0, v16
	v_fma_f32 v0, s4, v35, v114
	v_mul_f32_e32 v0, v0, v4
	v_exp_f32_e32 v0, v0
	s_waitcnt vmcnt(5)
	v_add_f32_e32 v1, v1, v121
	s_waitcnt lgkmcnt(4)
	v_fmac_f32_e32 v115, v38, v20
	s_waitcnt lgkmcnt(3)
	v_fmac_f32_e32 v116, v42, v20
	v_add_f32_e32 v0, 1.0, v0
	v_rcp_f32_e32 v0, v0
	s_waitcnt lgkmcnt(0)
	v_fmac_f32_e32 v119, v54, v20
	v_fmac_f32_e32 v117, v46, v20
	v_fmac_f32_e32 v118, v50, v20
	v_mul_f32_e32 v21, v1, v0
	v_fma_f32 v0, s4, v36, v114
	v_fma_f32 v1, v112, v36, v113
	v_mul_f32_e32 v0, v0, v1
	v_exp_f32_e32 v0, v0
	v_fmamk_f32 v1, v6, 0x39800000, v2
	s_waitcnt vmcnt(4)
	v_add_f32_e32 v1, v1, v126
	v_fmac_f32_e32 v115, v39, v21
	v_add_f32_e32 v0, 1.0, v0
	v_rcp_f32_e32 v0, v0
	v_lshlrev_b32_e32 v39, 2, v34
	v_fmac_f32_e32 v116, v43, v21
	v_or_b32_e32 v4, 0x10400, v39
	v_mul_f32_e32 v22, v1, v0
	v_fma_f32 v0, s4, v37, v114
	v_fma_f32 v1, v112, v37, v113
	v_mul_f32_e32 v0, v0, v1
	v_exp_f32_e32 v0, v0
	s_waitcnt vmcnt(3)
	v_add_f32_e32 v1, v3, v103
	s_add_u32 s40, s8, 0xc0000
	s_addc_u32 s41, s9, 0
	global_load_dword v103, v96, s[40:41] nt
	v_fmac_f32_e32 v115, v40, v22
	v_fmac_f32_e32 v119, v55, v21
	v_add_f32_e32 v0, 1.0, v0
	v_rcp_f32_e32 v0, v0
	v_fmac_f32_e32 v117, v47, v21
	v_fmac_f32_e32 v118, v51, v21
	v_fmac_f32_e32 v119, v56, v22
	v_mul_f32_e32 v23, v1, v0
	v_or_b32_e32 v0, 0x10000, v39
	v_fmac_f32_e32 v115, v41, v23
	ds_read_b128 v[0:3], v0
	ds_read_b128 v[40:43], v4
	v_fmac_f32_e32 v116, v44, v22
	v_fmac_f32_e32 v117, v48, v22
	v_fmac_f32_e32 v118, v52, v22
	v_fmac_f32_e32 v119, v57, v23
	v_or_b32_e32 v35, 0x10800, v39
	v_or_b32_e32 v36, 0x10c00, v39
	v_or_b32_e32 v37, 0x11000, v39
	v_or_b32_e32 v38, 0x11400, v39
	s_waitcnt lgkmcnt(0)
	v_fma_f32 v57, s4, v41, v114
	v_fma_f32 v58, v112, v41, v113
	v_or_b32_e32 v41, 0x11800, v39
	v_mov_b32_e32 v39, v96
	v_fmac_f32_e32 v116, v45, v23
	v_fmac_f32_e32 v117, v49, v23
	v_fmac_f32_e32 v118, v53, v23
	ds_read_b128 v[16:19], v35
	ds_read_b128 v[4:7], v36
	v_fma_f32 v59, s4, v42, v114
	v_fma_f32 v94, v112, v42, v113
	ds_read_b128 v[44:47], v37
	ds_read_b128 v[48:51], v38
	ds_read_b128 v[52:55], v41
	v_fma_f32 v56, s4, v40, v114
	s_add_u32 s40, s8, 0xe0000
	s_addc_u32 s41, s9, 0
	global_load_dword v120, v96, s[40:41] nt
	s_add_u32 s40, s8, 0xe4000
	s_addc_u32 s41, s9, 0
	global_load_dword v121, v96, s[40:41] nt
	s_add_u32 s40, s8, 0xe8000
	s_addc_u32 s41, s9, 0
	global_load_dword v126, v96, s[40:41] nt
	v_fma_f32 v40, v112, v40, v113
	v_fmamk_f32 v0, v8, 0x39800000, v0
	v_mul_f32_e32 v8, v56, v40
	v_exp_f32_e32 v8, v8
	v_fma_f32 v95, s4, v43, v114
	v_fma_f32 v43, v112, v43, v113
	v_fmac_f32_e32 v3, 0x39800000, v11
	v_add_f32_e32 v8, 1.0, v8
	v_rcp_f32_e32 v8, v8
	s_waitcnt vmcnt(3)
	v_add_f32_e32 v0, v0, v103
	s_add_u32 s40, s8, 0xec000
	s_addc_u32 s41, s9, 0
	global_load_dword v103, v96, s[40:41] nt
	v_mul_f32_e32 v42, v0, v8
	v_fmamk_f32 v0, v9, 0x39800000, v1
	v_mul_f32_e32 v1, v57, v58
	v_exp_f32_e32 v1, v1
	v_add_f32_e32 v0, v0, v100
	s_waitcnt lgkmcnt(4)
	v_fmac_f32_e32 v115, v16, v42
	s_waitcnt lgkmcnt(2)
	v_fmac_f32_e32 v117, v44, v42
	v_add_f32_e32 v1, 1.0, v1
	v_rcp_f32_e32 v1, v1
	s_waitcnt lgkmcnt(1)
	v_fmac_f32_e32 v118, v48, v42
	v_or_b32_e32 v44, 56, v97
	v_fmac_f32_e32 v116, v4, v42
	v_mul_f32_e32 v40, v0, v1
	v_mul_f32_e32 v1, v59, v94
	v_exp_f32_e32 v1, v1
	v_fmamk_f32 v0, v10, 0x39800000, v2
	v_add_f32_e32 v0, v0, v101
	v_fmac_f32_e32 v115, v17, v40
	v_add_f32_e32 v1, 1.0, v1
	v_rcp_f32_e32 v1, v1
	v_fmac_f32_e32 v118, v49, v40
	v_lshlrev_b32_e32 v49, 2, v44
	v_or_b32_e32 v4, 0x10400, v49
	v_mul_f32_e32 v39, v0, v1
	v_mul_f32_e32 v0, v95, v43
	v_exp_f32_e32 v0, v0
	v_add_f32_e32 v1, v3, v102
	v_fmac_f32_e32 v115, v18, v39
	s_waitcnt lgkmcnt(0)
	v_fmac_f32_e32 v119, v52, v42
	v_add_f32_e32 v0, 1.0, v0
	v_rcp_f32_e32 v0, v0
	v_fmac_f32_e32 v117, v45, v40
	v_fmac_f32_e32 v116, v5, v40
	v_fmac_f32_e32 v119, v53, v40
	v_mul_f32_e32 v43, v1, v0
	v_or_b32_e32 v0, 0x10000, v49
	v_fmac_f32_e32 v115, v19, v43
	ds_read_b128 v[0:3], v0
	ds_read_b128 v[16:19], v4
	v_fmac_f32_e32 v117, v46, v39
	v_fmac_f32_e32 v116, v6, v39
	v_fmac_f32_e32 v118, v50, v39
	v_fmac_f32_e32 v119, v54, v39
	v_fmac_f32_e32 v117, v47, v43
	v_or_b32_e32 v45, 0x10800, v49
	v_or_b32_e32 v46, 0x10c00, v49
	v_or_b32_e32 v47, 0x11000, v49
	v_or_b32_e32 v48, 0x11400, v49
	v_or_b32_e32 v49, 0x11800, v49
	v_mov_b32_e32 v58, v96
	v_fmac_f32_e32 v116, v7, v43
	v_fmac_f32_e32 v118, v51, v43
	v_fmac_f32_e32 v119, v55, v43
	ds_read_b128 v[8:11], v45
	ds_read_b128 v[4:7], v46
	s_waitcnt lgkmcnt(3)
	v_fmamk_f32 v0, v12, 0x39800000, v0
	v_fmamk_f32 v1, v13, 0x39800000, v1
	v_fmamk_f32 v2, v14, 0x39800000, v2
	v_fmac_f32_e32 v3, 0x39800000, v15
	ds_read_b128 v[12:15], v47
	ds_read_b128 v[50:53], v48
	ds_read_b128 v[54:57], v49
	s_waitcnt lgkmcnt(5)
	v_fma_f32 v95, s4, v16, v114
	v_fma_f32 v16, v112, v16, v113
	v_mul_f32_e32 v16, v95, v16
	v_exp_f32_e32 v16, v16
	s_waitcnt vmcnt(3)
	v_add_f32_e32 v0, v0, v120
	v_add_f32_e32 v16, 1.0, v16
	v_rcp_f32_e32 v16, v16
	s_waitcnt vmcnt(2)
	v_add_f32_e32 v1, v1, v121
	v_mul_f32_e32 v16, v0, v16
	v_fma_f32 v0, s4, v17, v114
	v_fma_f32 v17, v112, v17, v113
	v_mul_f32_e32 v0, v0, v17
	v_exp_f32_e32 v0, v0
	s_waitcnt lgkmcnt(4)
	v_fmac_f32_e32 v115, v8, v16
	s_waitcnt lgkmcnt(3)
	v_fmac_f32_e32 v116, v4, v16
	s_waitcnt lgkmcnt(2)
	v_fmac_f32_e32 v117, v12, v16
	v_add_f32_e32 v0, 1.0, v0
	v_rcp_f32_e32 v0, v0
	s_waitcnt lgkmcnt(1)
	v_fmac_f32_e32 v118, v50, v16
	s_waitcnt lgkmcnt(0)
	v_fmac_f32_e32 v119, v54, v16
	v_mul_f32_e32 v17, v1, v0
	v_fma_f32 v0, s4, v18, v114
	v_fma_f32 v1, v112, v18, v113
	v_mul_f32_e32 v0, v0, v1
	v_exp_f32_e32 v0, v0
	s_waitcnt vmcnt(1)
	v_add_f32_e32 v1, v2, v126
	v_fmac_f32_e32 v114, s4, v19
	v_fmac_f32_e32 v113, v112, v19
	v_add_f32_e32 v0, 1.0, v0
	v_rcp_f32_e32 v0, v0
	v_fmac_f32_e32 v115, v9, v17
	v_fmac_f32_e32 v116, v5, v17
	v_fmac_f32_e32 v117, v13, v17
	v_mul_f32_e32 v18, v1, v0
	v_mul_f32_e32 v0, v114, v113
	v_exp_f32_e32 v0, v0
	s_waitcnt vmcnt(0)
	v_add_f32_e32 v1, v3, v103
	v_fmac_f32_e32 v118, v51, v17
	v_fmac_f32_e32 v119, v55, v17
	v_add_f32_e32 v0, 1.0, v0
	v_rcp_f32_e32 v0, v0
	v_fmac_f32_e32 v115, v10, v18
	v_fmac_f32_e32 v116, v6, v18
	v_fmac_f32_e32 v117, v14, v18
	v_mul_f32_e32 v19, v1, v0
	v_mbcnt_lo_u32_b32 v0, -1, 0
	v_mbcnt_hi_u32_b32 v0, -1, v0
	v_and_b32_e32 v2, 64, v0
	v_xor_b32_e32 v1, 32, v0
	v_add_u32_e32 v2, 64, v2
	v_cmp_lt_i32_e32 vcc, v1, v2
	v_fmac_f32_e32 v118, v52, v18
	v_fmac_f32_e32 v119, v56, v18
	v_cndmask_b32_e32 v0, v0, v1, vcc
	v_fmac_f32_e32 v115, v11, v19
	v_fmac_f32_e32 v116, v7, v19
	v_fmac_f32_e32 v117, v15, v19
	v_fmac_f32_e32 v118, v53, v19
	v_fmac_f32_e32 v119, v57, v19
	v_lshlrev_b32_e32 v50, 2, v0
	ds_bpermute_b32 v0, v50, v115
	ds_bpermute_b32 v1, v50, v116
	ds_bpermute_b32 v2, v50, v117
	ds_bpermute_b32 v3, v50, v118
	ds_bpermute_b32 v4, v50, v119
	v_cmp_gt_u32_e32 vcc, 32, v109
	s_and_saveexec_b64 s[4:5], vcc
	s_cbranch_execz .LBB13_8
	s_mul_i32 s7, s14, 0x280
	s_add_i32 s7, s6, s7
	s_waitcnt lgkmcnt(3)
	v_add_f32_e32 v1, v116, v1
	v_add_f32_e32 v0, v115, v0
	v_lshl_or_b32 v5, v98, 2, s7
	s_waitcnt lgkmcnt(0)
	v_add_f32_e32 v4, v119, v4
	v_add_f32_e32 v3, v118, v3
	v_add_f32_e32 v2, v117, v2
	ds_write2_b32 v5, v0, v1 offset1:32
	ds_write2_b32 v5, v2, v3 offset0:64 offset1:96
	ds_write_b32 v5, v4 offset:512

.LBB13_10:
	s_or_b64 exec, exec, s[4:5]
	s_waitcnt lgkmcnt(0)
	v_lshl_or_b32 v12, v98, 2, s6
	v_add_u32_e32 v14, 0x4800, v12
	s_barrier
	v_add_u32_e32 v10, 0x4000, v12
	v_add_u32_e32 v13, 0x4400, v12
	ds_read2_b32 v[0:1], v14 offset0:128 offset1:160
	ds_read2_b32 v[2:3], v13 offset0:192 offset1:224
	ds_read2_b32 v[4:5], v10 offset1:32
	ds_read2_b32 v[6:7], v10 offset0:192 offset1:224
	s_add_u32 s0, s0, s2
	s_waitcnt lgkmcnt(3)
	v_max_f32_e32 v8, v1, v1
	s_waitcnt lgkmcnt(2)
	v_max_f32_e32 v9, v2, v2
	v_max_f32_e32 v8, v9, v8
	s_waitcnt lgkmcnt(0)
	v_max3_f32 v15, v4, v7, v8
	v_sub_f32_e32 v4, v4, v15
	v_exp_f32_e32 v50, v4
	ds_read2_b32 v[8:9], v10 offset0:64 offset1:96
	ds_read2_b32 v[10:11], v10 offset0:128 offset1:160
	v_sub_f32_e32 v7, v7, v15
	v_fma_f32 v51, v5, v50, 0
	ds_read2_b32 v[4:5], v13 offset1:32
	v_exp_f32_e32 v54, v7
	s_waitcnt lgkmcnt(2)
	v_fma_f32 v52, v8, v50, 0
	v_sub_f32_e32 v2, v2, v15
	v_fma_f32 v53, v50, v9, 0
	s_waitcnt lgkmcnt(1)
	v_fma_f32 v10, v50, v10, 0
	ds_read2_b32 v[8:9], v13 offset0:64 offset1:96
	v_fma_f32 v11, v50, v11, 0
	v_fma_f32 v50, v50, v6, 0
	s_waitcnt lgkmcnt(1)
	v_fmac_f32_e32 v51, v4, v54
	v_fmac_f32_e32 v52, v5, v54
	ds_read2_b32 v[4:5], v13 offset0:128 offset1:160
	v_exp_f32_e32 v13, v2
	ds_read2_b32 v[6:7], v14 offset1:32
	v_sub_f32_e32 v1, v1, v15
	s_waitcnt lgkmcnt(2)
	v_fmac_f32_e32 v53, v54, v8
	v_fmac_f32_e32 v51, v3, v13
	ds_read2_b32 v[2:3], v14 offset0:192 offset1:224
	s_waitcnt lgkmcnt(1)
	v_fmac_f32_e32 v52, v6, v13
	v_exp_f32_e32 v6, v1
	v_fmac_f32_e32 v10, v54, v9
	ds_read2_b32 v[8:9], v14 offset0:64 offset1:96
	v_fmac_f32_e32 v50, v54, v5
	v_add_u32_e32 v1, 0x4c00, v12
	s_waitcnt lgkmcnt(1)
	v_fmac_f32_e32 v51, v2, v6
	s_mov_b32 s4, 0x3f317218
	s_addc_u32 s1, s1, s3
	v_fmac_f32_e32 v11, v54, v4
	ds_read2_b32 v[4:5], v1 offset1:32
	v_fmac_f32_e32 v50, v13, v0
	ds_read2_b32 v[0:1], v1 offset0:64 offset1:96
	v_div_scale_f32 v2, s[2:3], v51, v51, s4
	v_fmac_f32_e32 v52, v3, v6
	v_rcp_f32_e32 v3, v2
	s_waitcnt lgkmcnt(2)
	v_fmac_f32_e32 v11, v13, v9
	s_waitcnt lgkmcnt(0)
	v_fmac_f32_e32 v11, v6, v0
	v_fmac_f32_e32 v53, v13, v7
	v_fma_f32 v0, -v2, v3, 1.0
	v_fmac_f32_e32 v3, v0, v3
	v_div_scale_f32 v0, vcc, s4, v51, s4
	v_fmac_f32_e32 v50, v6, v1
	v_mul_f32_e32 v1, v0, v3
	v_fmac_f32_e32 v53, v6, v4
	v_fma_f32 v4, -v2, v1, v0
	v_fmac_f32_e32 v1, v4, v3
	v_fma_f32 v0, -v2, v1, v0
	v_fmac_f32_e32 v10, v13, v8
	v_div_fmas_f32 v0, v0, v3, v1
	v_fmac_f32_e32 v10, v6, v5
	v_div_fixup_f32 v0, v0, v51, s4
	v_mul_f32_e32 v2, v52, v0
	v_mul_f32_e32 v4, v53, v0
	v_mul_f32_e32 v3, v10, v0
	v_mul_f32_e32 v1, v11, v0
	v_mul_f32_e32 v0, v50, v0
	ds_read_b128 v[6:9], v99
	ds_read_b128 v[10:13], v122
	ds_read_b128 v[50:53], v123
	ds_read_b128 v[54:57], v125
	v_mov_b32_e32 v5, 0x11c00
	v_lshl_or_b32 v14, v97, 2, v5
	ds_read_b128 v[98:101], v124
	ds_read_b128 v[112:115], v14
	s_waitcnt lgkmcnt(4)
	v_mul_f32_e32 v10, v4, v10
	v_fmac_f32_e32 v10, v2, v6
	s_waitcnt lgkmcnt(3)
	v_fmac_f32_e32 v10, v3, v50
	s_waitcnt lgkmcnt(2)
	v_fmac_f32_e32 v10, v1, v54
	s_waitcnt lgkmcnt(1)
	v_fmac_f32_e32 v10, v0, v98
	s_waitcnt lgkmcnt(0)
	v_add_f32_e32 v6, v112, v10
	v_mov_b32_e32 v14, v96
	v_add_f32_e32 v6, v110, v6
	global_store_dword v14, v6, s[0:1] nt
	v_fma_f32 v6, v4, v11, v72
	v_fmac_f32_e32 v6, v2, v7
	v_fmac_f32_e32 v6, v3, v51
	v_fmac_f32_e32 v6, v1, v55
	v_fmac_f32_e32 v6, v0, v99
	v_add_f32_e32 v6, v113, v6
	s_add_u32 s40, s0, 0x4000
	s_addc_u32 s41, s1, 0
	global_store_dword v14, v6, s[40:41] nt
	v_fma_f32 v6, v4, v12, v73
	v_fmac_f32_e32 v6, v2, v8
	v_fmac_f32_e32 v6, v3, v52
	v_fmac_f32_e32 v6, v1, v56
	v_fmac_f32_e32 v6, v0, v100
	v_add_f32_e32 v6, v114, v6
	s_add_u32 s40, s0, 0x8000
	s_addc_u32 s41, s1, 0
	global_store_dword v14, v6, s[40:41] nt
	v_fma_f32 v6, v4, v13, v74
	v_fmac_f32_e32 v6, v2, v9
	v_fmac_f32_e32 v6, v3, v53
	v_fmac_f32_e32 v6, v1, v57
	v_fmac_f32_e32 v6, v0, v101
	v_add_f32_e32 v6, v115, v6
	s_add_u32 s40, s0, 0xc000
	s_addc_u32 s41, s1, 0
	global_store_dword v14, v6, s[40:41] nt
	ds_read_b128 v[6:9], v104
	ds_read_b128 v[10:13], v105
	ds_read_b128 v[50:53], v106
	ds_read_b128 v[54:57], v107
	v_lshl_or_b32 v14, v84, 2, v5
	ds_read_b128 v[98:101], v108
	ds_read_b128 v[102:105], v14
	s_waitcnt lgkmcnt(4)
	v_fma_f32 v10, v4, v10, v76
	v_fmac_f32_e32 v10, v2, v6
	s_waitcnt lgkmcnt(3)
	v_fmac_f32_e32 v10, v3, v50
	s_waitcnt lgkmcnt(2)
	v_fmac_f32_e32 v10, v1, v54
	s_waitcnt lgkmcnt(1)
	v_fmac_f32_e32 v10, v0, v98
	v_mov_b32_e32 v14, v96
	s_waitcnt lgkmcnt(0)
	v_add_f32_e32 v6, v102, v10
	s_add_u32 s40, s0, 0x20000
	s_addc_u32 s41, s1, 0
	global_store_dword v14, v6, s[40:41] nt
	v_fma_f32 v6, v4, v11, v75
	v_fmac_f32_e32 v6, v2, v7
	v_fmac_f32_e32 v6, v3, v51
	v_fmac_f32_e32 v6, v1, v55
	v_fmac_f32_e32 v6, v0, v99
	v_add_f32_e32 v6, v103, v6
	s_add_u32 s40, s0, 0x24000
	s_addc_u32 s41, s1, 0
	global_store_dword v14, v6, s[40:41] nt
	v_fma_f32 v6, v4, v12, v85
	v_fmac_f32_e32 v6, v2, v8
	v_fmac_f32_e32 v6, v3, v52
	v_fmac_f32_e32 v6, v1, v56
	v_fmac_f32_e32 v6, v0, v100
	v_add_f32_e32 v6, v104, v6
	s_add_u32 s40, s0, 0x28000
	s_addc_u32 s41, s1, 0
	global_store_dword v14, v6, s[40:41] nt
	v_fma_f32 v6, v4, v13, v83
	v_fmac_f32_e32 v6, v2, v9
	v_fmac_f32_e32 v6, v3, v53
	v_fmac_f32_e32 v6, v1, v57
	v_fmac_f32_e32 v6, v0, v101
	v_add_f32_e32 v6, v105, v6
	s_add_u32 s40, s0, 0x2c000
	s_addc_u32 s41, s1, 0
	global_store_dword v14, v6, s[40:41] nt
	ds_read_b128 v[6:9], v78
	ds_read_b128 v[10:13], v79
	ds_read_b128 v[50:53], v80
	ds_read_b128 v[54:57], v81
	v_lshl_or_b32 v14, v77, 2, v5
	ds_read_b128 v[72:75], v82
	ds_read_b128 v[76:79], v14
	s_waitcnt lgkmcnt(4)
	v_fma_f32 v10, v4, v10, v68
	v_fmac_f32_e32 v10, v2, v6
	s_waitcnt lgkmcnt(3)
	v_fmac_f32_e32 v10, v3, v50
	s_waitcnt lgkmcnt(2)
	v_fmac_f32_e32 v10, v1, v54
	s_waitcnt lgkmcnt(1)
	v_fmac_f32_e32 v10, v0, v72
	v_mov_b32_e32 v14, v96
	s_waitcnt lgkmcnt(0)
	v_add_f32_e32 v6, v76, v10
	s_add_u32 s40, s0, 0x40000
	s_addc_u32 s41, s1, 0
	global_store_dword v14, v6, s[40:41] nt
	v_fma_f32 v6, v4, v11, v60
	v_fmac_f32_e32 v6, v2, v7
	v_fmac_f32_e32 v6, v3, v51
	v_fmac_f32_e32 v6, v1, v55
	v_fmac_f32_e32 v6, v0, v73
	v_add_f32_e32 v6, v77, v6
	s_add_u32 s40, s0, 0x44000
	s_addc_u32 s41, s1, 0
	global_store_dword v14, v6, s[40:41] nt
	v_fma_f32 v6, v4, v12, v64
	v_fmac_f32_e32 v6, v2, v8
	v_fmac_f32_e32 v6, v3, v52
	v_fmac_f32_e32 v6, v1, v56
	v_fmac_f32_e32 v6, v0, v74
	v_add_f32_e32 v6, v78, v6
	s_add_u32 s40, s0, 0x48000
	s_addc_u32 s41, s1, 0
	global_store_dword v14, v6, s[40:41] nt
	v_fma_f32 v6, v4, v13, v61
	v_fmac_f32_e32 v6, v2, v9
	v_fmac_f32_e32 v6, v3, v53
	v_fmac_f32_e32 v6, v1, v57
	v_fmac_f32_e32 v6, v0, v75
	v_add_f32_e32 v6, v79, v6
	s_add_u32 s40, s0, 0x4c000
	s_addc_u32 s41, s1, 0
	global_store_dword v14, v6, s[40:41] nt
	ds_read_b128 v[6:9], v63
	ds_read_b128 v[10:13], v65
	ds_read_b128 v[50:53], v66
	ds_read_b128 v[54:57], v67
	v_lshl_or_b32 v14, v62, 2, v5
	ds_read_b128 v[58:61], v69
	ds_read_b128 v[62:65], v14
	s_waitcnt lgkmcnt(4)
	v_fma_f32 v10, v4, v10, v71
	v_fmac_f32_e32 v10, v2, v6
	s_waitcnt lgkmcnt(3)
	v_fmac_f32_e32 v10, v3, v50
	s_waitcnt lgkmcnt(2)
	v_fmac_f32_e32 v10, v1, v54
	s_waitcnt lgkmcnt(1)
	v_fmac_f32_e32 v10, v0, v58
	v_mov_b32_e32 v14, v96
	s_waitcnt lgkmcnt(0)
	v_add_f32_e32 v6, v62, v10
	s_add_u32 s40, s0, 0x60000
	s_addc_u32 s41, s1, 0
	global_store_dword v14, v6, s[40:41] nt
	v_fma_f32 v6, v4, v11, v70
	v_fmac_f32_e32 v6, v2, v7
	v_fmac_f32_e32 v6, v3, v51
	v_fmac_f32_e32 v6, v1, v55
	v_fmac_f32_e32 v6, v0, v59
	v_add_f32_e32 v6, v63, v6
	s_add_u32 s40, s0, 0x64000
	s_addc_u32 s41, s1, 0
	global_store_dword v14, v6, s[40:41] nt
	v_fma_f32 v6, v4, v12, v88
	v_fmac_f32_e32 v6, v2, v8
	v_fmac_f32_e32 v6, v3, v52
	v_fmac_f32_e32 v6, v1, v56
	v_fmac_f32_e32 v6, v0, v60
	v_add_f32_e32 v6, v64, v6
	s_add_u32 s40, s0, 0x68000
	s_addc_u32 s41, s1, 0
	global_store_dword v14, v6, s[40:41] nt
	v_fma_f32 v6, v4, v13, v86
	v_fmac_f32_e32 v6, v2, v9
	v_fmac_f32_e32 v6, v3, v53
	v_fmac_f32_e32 v6, v1, v57
	v_fmac_f32_e32 v6, v0, v61
	v_add_f32_e32 v6, v65, v6
	s_add_u32 s40, s0, 0x6c000
	s_addc_u32 s41, s1, 0
	global_store_dword v14, v6, s[40:41] nt
	ds_read_b128 v[6:9], v89
	ds_read_b128 v[10:13], v90
	ds_read_b128 v[50:53], v91
	ds_read_b128 v[54:57], v92
	v_lshl_or_b32 v14, v87, 2, v5
	ds_read_b128 v[58:61], v93
	ds_read_b128 v[62:65], v14
	s_waitcnt lgkmcnt(4)
	v_fma_f32 v10, v4, v10, v25
	v_fmac_f32_e32 v10, v2, v6
	s_waitcnt lgkmcnt(3)
	v_fmac_f32_e32 v10, v3, v50
	s_waitcnt lgkmcnt(2)
	v_fmac_f32_e32 v10, v1, v54
	s_waitcnt lgkmcnt(1)
	v_fmac_f32_e32 v10, v0, v58
	v_mov_b32_e32 v14, v96
	s_waitcnt lgkmcnt(0)
	v_add_f32_e32 v6, v62, v10
	s_add_u32 s40, s0, 0x80000
	s_addc_u32 s41, s1, 0
	global_store_dword v14, v6, s[40:41] nt
	v_fma_f32 v6, v4, v11, v24
	v_fmac_f32_e32 v6, v2, v7
	v_fmac_f32_e32 v6, v3, v51
	v_fmac_f32_e32 v6, v1, v55
	v_fmac_f32_e32 v6, v0, v59
	v_add_f32_e32 v6, v63, v6
	s_add_u32 s40, s0, 0x84000
	s_addc_u32 s41, s1, 0
	global_store_dword v14, v6, s[40:41] nt
	v_fma_f32 v6, v4, v12, v28
	v_fmac_f32_e32 v6, v2, v8
	v_fmac_f32_e32 v6, v3, v52
	v_fmac_f32_e32 v6, v1, v56
	v_fmac_f32_e32 v6, v0, v60
	v_add_f32_e32 v6, v64, v6
	s_add_u32 s40, s0, 0x88000
	s_addc_u32 s41, s1, 0
	global_store_dword v14, v6, s[40:41] nt
	v_fma_f32 v6, v4, v13, v26
	v_fmac_f32_e32 v6, v2, v9
	v_fmac_f32_e32 v6, v3, v53
	v_fmac_f32_e32 v6, v1, v57
	v_fmac_f32_e32 v6, v0, v61
	v_add_f32_e32 v6, v65, v6
	s_add_u32 s40, s0, 0x8c000
	s_addc_u32 s41, s1, 0
	global_store_dword v14, v6, s[40:41] nt
	ds_read_b128 v[6:9], v29
	ds_read_b128 v[10:13], v30
	ds_read_b128 v[28:31], v31
	ds_read_b128 v[50:53], v32
	v_lshl_or_b32 v14, v27, 2, v5
	ds_read_b128 v[24:27], v33
	ds_read_b128 v[54:57], v14
	s_waitcnt lgkmcnt(4)
	v_fma_f32 v10, v4, v10, v20
	v_fmac_f32_e32 v10, v2, v6
	s_waitcnt lgkmcnt(3)
	v_fmac_f32_e32 v10, v3, v28
	s_waitcnt lgkmcnt(2)
	v_fmac_f32_e32 v10, v1, v50
	s_waitcnt lgkmcnt(1)
	v_fmac_f32_e32 v10, v0, v24
	v_mov_b32_e32 v14, v96
	s_waitcnt lgkmcnt(0)
	v_add_f32_e32 v6, v54, v10
	s_add_u32 s40, s0, 0xa0000
	s_addc_u32 s41, s1, 0
	global_store_dword v14, v6, s[40:41] nt
	v_fma_f32 v6, v4, v11, v21
	v_fmac_f32_e32 v6, v2, v7
	v_fmac_f32_e32 v6, v3, v29
	v_fmac_f32_e32 v6, v1, v51
	v_fmac_f32_e32 v6, v0, v25
	v_add_f32_e32 v6, v55, v6
	s_add_u32 s40, s0, 0xa4000
	s_addc_u32 s41, s1, 0
	global_store_dword v14, v6, s[40:41] nt
	v_fma_f32 v6, v4, v12, v22
	v_fmac_f32_e32 v6, v2, v8
	v_fmac_f32_e32 v6, v3, v30
	v_fmac_f32_e32 v6, v1, v52
	v_fmac_f32_e32 v6, v0, v26
	v_add_f32_e32 v6, v56, v6
	s_add_u32 s40, s0, 0xa8000
	s_addc_u32 s41, s1, 0
	global_store_dword v14, v6, s[40:41] nt
	v_fma_f32 v6, v4, v13, v23
	v_fmac_f32_e32 v6, v2, v9
	v_fmac_f32_e32 v6, v3, v31
	v_fmac_f32_e32 v6, v1, v53
	v_fmac_f32_e32 v6, v0, v27
	v_add_f32_e32 v6, v57, v6
	s_add_u32 s40, s0, 0xac000
	s_addc_u32 s41, s1, 0
	global_store_dword v14, v6, s[40:41] nt
	ds_read_b128 v[6:9], v35
	ds_read_b128 v[10:13], v36
	ds_read_b128 v[20:23], v37
	ds_read_b128 v[24:27], v38
	v_lshl_or_b32 v14, v34, 2, v5
	ds_read_b128 v[28:31], v41
	ds_read_b128 v[32:35], v14
	s_waitcnt lgkmcnt(4)
	v_fma_f32 v10, v4, v10, v42
	v_fmac_f32_e32 v10, v2, v6
	s_waitcnt lgkmcnt(3)
	v_fmac_f32_e32 v10, v3, v20
	s_waitcnt lgkmcnt(2)
	v_fmac_f32_e32 v10, v1, v24
	s_waitcnt lgkmcnt(1)
	v_fmac_f32_e32 v10, v0, v28
	v_mov_b32_e32 v14, v96
	s_waitcnt lgkmcnt(0)
	v_add_f32_e32 v6, v32, v10
	s_add_u32 s40, s0, 0xc0000
	s_addc_u32 s41, s1, 0
	global_store_dword v14, v6, s[40:41] nt
	v_fma_f32 v6, v4, v11, v40
	v_fmac_f32_e32 v6, v2, v7
	v_fmac_f32_e32 v6, v3, v21
	v_fmac_f32_e32 v6, v1, v25
	v_fmac_f32_e32 v6, v0, v29
	v_add_f32_e32 v6, v33, v6
	s_add_u32 s40, s0, 0xc4000
	s_addc_u32 s41, s1, 0
	global_store_dword v14, v6, s[40:41] nt
	v_fma_f32 v6, v4, v12, v39
	v_fmac_f32_e32 v6, v2, v8
	v_fmac_f32_e32 v6, v3, v22
	v_fmac_f32_e32 v6, v1, v26
	v_fmac_f32_e32 v6, v0, v30
	v_add_f32_e32 v6, v34, v6
	s_add_u32 s40, s0, 0xc8000
	s_addc_u32 s41, s1, 0
	global_store_dword v14, v6, s[40:41] nt
	v_fma_f32 v6, v4, v13, v43
	v_fmac_f32_e32 v6, v2, v9
	v_fmac_f32_e32 v6, v3, v23
	v_fmac_f32_e32 v6, v1, v27
	v_fmac_f32_e32 v6, v0, v31
	v_add_f32_e32 v6, v35, v6
	s_add_u32 s40, s0, 0xcc000
	s_addc_u32 s41, s1, 0
	global_store_dword v14, v6, s[40:41] nt
	ds_read_b128 v[6:9], v45
	ds_read_b128 v[10:13], v46
	ds_read_b128 v[20:23], v47
	ds_read_b128 v[24:27], v48
	v_lshl_or_b32 v5, v44, 2, v5
	ds_read_b128 v[28:31], v49
	ds_read_b128 v[32:35], v5
	s_waitcnt lgkmcnt(4)
	v_fma_f32 v5, v4, v10, v16
	v_fmac_f32_e32 v5, v2, v6
	s_waitcnt lgkmcnt(3)
	v_fmac_f32_e32 v5, v3, v20
	s_waitcnt lgkmcnt(2)
	v_fmac_f32_e32 v5, v1, v24
	s_waitcnt lgkmcnt(1)
	v_fmac_f32_e32 v5, v0, v28
	s_waitcnt lgkmcnt(0)
	v_add_f32_e32 v5, v32, v5
	s_add_u32 s40, s0, 0xe0000
	s_addc_u32 s41, s1, 0
	global_store_dword v96, v5, s[40:41] nt
	v_fma_f32 v5, v4, v11, v17
	v_fmac_f32_e32 v5, v2, v7
	v_fmac_f32_e32 v5, v3, v21
	v_fmac_f32_e32 v5, v1, v25
	v_fmac_f32_e32 v5, v0, v29
	v_add_f32_e32 v5, v33, v5
	s_add_u32 s40, s0, 0xe4000
	s_addc_u32 s41, s1, 0
	global_store_dword v96, v5, s[40:41] nt
	v_mul_f32_e32 v5, v4, v12
	v_mul_f32_e32 v4, v4, v13
	v_fmac_f32_e32 v5, v2, v8
	v_fmac_f32_e32 v4, v2, v9
	v_fmac_f32_e32 v5, v3, v22
	v_fmac_f32_e32 v4, v3, v23
	v_fmac_f32_e32 v5, v1, v26
	v_fmac_f32_e32 v4, v1, v27
	v_fmac_f32_e32 v5, v0, v30
	v_fmac_f32_e32 v4, v0, v31
	v_add_f32_e32 v5, v34, v5
	v_add_f32_e32 v0, v35, v4
	v_add_f32_e32 v5, v18, v5
	v_add_u32_e32 v6, 0xe8000, v96
	v_add_f32_e32 v0, v19, v0
	v_add_u32_e32 v1, 0xec000, v96
	global_store_dword v6, v5, s[0:1] nt
	global_store_dword v1, v0, s[0:1] nt
	s_endpgm
